# P9: cooperative L2 prefetch in the peeled first K-iteration (B slab share k-tiles 4-9 by waves 0-2, gathered A rows k-tiles 4-8 by waves 3-7)
# baseline (speedup 1.0000x reference)
.LBB0_1362:
	s_and_b64 vcc, exec, s[0:1]
	s_cmp_eq_u32 s101, 0
	s_cbranch_scc1 .Lgk_first_p9
	v_mov_b32_e32 v175, v169
	v_mov_b32_e32 v173, v169
	s_mov_b32 s21, 0
	s_mov_b64 s[30:31], 0x100
	s_mov_b64 s[34:35], s[14:15]
	v_readfirstlane_b32 s74, v0
	s_lshr_b32 s74, s74, 6
	s_bfe_u32 s75, s33, 0x30002
	s_lshl_b32 s75, s75, 16
	s_lshl_b32 s76, s74, 8
	s_add_u32 s75, s75, s76
	s_add_u32 s75, s75, 0x200
	s_add_u32 s76, s28, s75
	s_addc_u32 s77, s29, 0
	s_add_u32 s75, s74, 1
	s_lshl_b32 s75, s75, 7
	s_add_u32 s78, s8, s75
	s_addc_u32 s79, s9, 0
	s_cmp_lt_u32 s74, 3
	s_cselect_b64 s[76:77], s[76:77], s[78:79]
	s_cselect_b64 s[78:79], -1, 0
	v_and_b32_e32 v249, 31, v206
	v_lshrrev_b32_e32 v250, 5, v206
	v_lshlrev_b32_e32 v249, 11, v249
	v_lshl_or_b32 v249, v250, 7, v249
	s_sub_u32 s75, s48, 1
	s_lshl_b32 s75, s75, 10
	s_add_u32 s75, s75, 0x20000
	s_lshl_b32 s73, s26, 8
	s_add_u32 s75, s75, s73
	v_lshl_add_u32 v250, v206, 2, s75
	ds_read_b32 v250, v250
	ds_read_b128 v[26:29], v191
	ds_read_b128 v[30:33], v191 offset:1024
	ds_read_b128 v[18:21], v191 offset:2048
	ds_read_b128 v[22:25], v191 offset:3072
	ds_read_b128 v[10:13], v192
	ds_read_b128 v[14:17], v192 offset:1024
	ds_read_b128 v[2:5], v192 offset:2048
	ds_read_b128 v[6:9], v192 offset:3072
	s_cmp_eq_u32 s55, s21
	s_cselect_b64 vcc, -1, 0
	s_add_i32 s21, s21, 2
	s_and_b64 s[36:37], vcc, exec
	s_cselect_b32 s36, 0, s30
	s_cselect_b32 s23, 0, s31
	s_add_u32 s36, s8, s36
	s_addc_u32 s37, s9, s23
	s_add_u32 s23, s28, s30
	s_addc_u32 s70, s29, s31
	s_and_b64 s[38:39], vcc, exec
	v_cndmask_b32_e32 v168, v197, v198, vcc
	v_cndmask_b32_e32 v202, v172, v200, vcc
	v_cndmask_b32_e32 v184, v170, v199, vcc
	s_cselect_b32 s39, s25, s70
	s_cselect_b32 s38, s24, s23
	s_mov_b32 m0, s56
	v_lshl_add_u64 v[186:187], s[34:35], 0, v[172:173]
	ds_read_b128 v[176:179], v193
	ds_read_b128 v[180:183], v193 offset:1024
	ds_read_b128 v[208:211], v193 offset:2048
	ds_read_b128 v[212:215], v193 offset:3072
	ds_read_b128 v[216:219], v193 offset:4096
	ds_read_b128 v[220:223], v193 offset:5120
	ds_read_b128 v[224:227], v193 offset:6144
	ds_read_b128 v[228:231], v193 offset:7168
	global_load_lds_dwordx4 v[186:187], off
	v_lshl_add_u64 v[186:187], s[34:35], 0, v[174:175]
	s_mov_b32 m0, s57
	s_nop 0
	global_load_lds_dwordx4 v[186:187], off
	s_waitcnt vmcnt(16)
	s_waitcnt lgkmcnt(0)
	s_barrier
	s_setprio 1
	s_waitcnt lgkmcnt(0)
	v_mfma_scale_f32_16x16x128_f8f6f4 v[154:157], v[26:33], v[176:183], 0, v188, v189 op_sel_hi:[0,0,0]
	v_mfma_scale_f32_16x16x128_f8f6f4 v[150:153], v[18:25], v[176:183], 0, v188, v189 op_sel_hi:[0,0,0]
	v_mfma_scale_f32_16x16x128_f8f6f4 v[142:145], v[26:33], v[208:215], 0, v188, v189 op_sel_hi:[0,0,0]
	v_mfma_scale_f32_16x16x128_f8f6f4 v[134:137], v[18:25], v[208:215], 0, v188, v189 op_sel_hi:[0,0,0]
	v_mfma_scale_f32_16x16x128_f8f6f4 v[126:129], v[26:33], v[216:223], 0, v188, v189 op_sel_hi:[0,0,0]
	v_mfma_scale_f32_16x16x128_f8f6f4 v[118:121], v[18:25], v[216:223], 0, v188, v189 op_sel_hi:[0,0,0]
	v_mfma_scale_f32_16x16x128_f8f6f4 v[110:113], v[26:33], v[224:231], 0, v188, v189 op_sel_hi:[0,0,0]
	v_mfma_scale_f32_16x16x128_f8f6f4 v[102:105], v[18:25], v[224:231], 0, v188, v189 op_sel_hi:[0,0,0]
	s_setprio 0
	s_setprio 1
	v_mfma_scale_f32_16x16x128_f8f6f4 v[158:161], v[10:17], v[176:183], 0, v188, v189 op_sel_hi:[0,0,0]
	v_mfma_scale_f32_16x16x128_f8f6f4 v[146:149], v[2:9], v[176:183], 0, v188, v189 op_sel_hi:[0,0,0]
	v_mfma_scale_f32_16x16x128_f8f6f4 v[138:141], v[10:17], v[208:215], 0, v188, v189 op_sel_hi:[0,0,0]
	v_mfma_scale_f32_16x16x128_f8f6f4 v[130:133], v[2:9], v[208:215], 0, v188, v189 op_sel_hi:[0,0,0]
	v_mfma_scale_f32_16x16x128_f8f6f4 v[122:125], v[10:17], v[216:223], 0, v188, v189 op_sel_hi:[0,0,0]
	v_mfma_scale_f32_16x16x128_f8f6f4 v[114:117], v[2:9], v[216:223], 0, v188, v189 op_sel_hi:[0,0,0]
	v_mfma_scale_f32_16x16x128_f8f6f4 v[106:109], v[10:17], v[224:231], 0, v188, v189 op_sel_hi:[0,0,0]
	v_mfma_scale_f32_16x16x128_f8f6f4 v[98:101], v[2:9], v[224:231], 0, v188, v189 op_sel_hi:[0,0,0]
	s_setprio 0
	s_barrier
	s_mov_b32 m0, s58
	v_lshl_add_u64 v[176:177], s[38:39], 0, v[166:167]
	v_lshl_add_u64 v[178:179], s[38:39], 0, v[164:165]
	s_add_u32 s38, s38, s6
	ds_read_b128 v[208:211], v193 offset:16384
	ds_read_b128 v[212:215], v193 offset:17408
	ds_read_b128 v[216:219], v193 offset:18432
	ds_read_b128 v[220:223], v193 offset:19456
	ds_read_b128 v[224:227], v193 offset:20480
	ds_read_b128 v[228:231], v193 offset:21504
	ds_read_b128 v[232:235], v193 offset:22528
	ds_read_b128 v[236:239], v193 offset:23552
	global_load_lds_dwordx4 v[176:177], off
	s_mov_b32 m0, s59
	s_addc_u32 s39, s39, s7
	global_load_lds_dwordx4 v[178:179], off
	v_lshl_add_u64 v[180:181], s[38:39], 0, v[166:167]
	s_mov_b32 m0, s60
	v_lshl_add_u64 v[182:183], s[38:39], 0, v[164:165]
	global_load_lds_dwordx4 v[180:181], off
	s_mov_b32 m0, s61
	v_mov_b32_e32 v185, v169
	global_load_lds_dwordx4 v[182:183], off
	s_mov_b32 m0, s27
	v_lshl_add_u64 v[186:187], s[36:37], 0, v[168:169]
	global_load_lds_dwordx4 v168, s[36:37]
	s_mov_b32 m0, s45
	s_nop 0
	global_load_lds_dwordx4 v184, s[36:37]
	v_lshlrev_b32_e32 v250, 11, v250
	v_cndmask_b32_e64 v250, v250, v249, s[78:79]
	global_load_dword v251, v250, s[76:77]
	s_waitcnt vmcnt(17)
	s_waitcnt lgkmcnt(0)
	v_lshl_add_u64 v[184:185], s[36:37], 0, v[184:185]
	s_barrier
	s_setprio 1
	s_waitcnt lgkmcnt(0)
	v_mfma_scale_f32_16x16x128_f8f6f4 v[94:97], v[26:33], v[208:215], 0, v188, v189 op_sel_hi:[0,0,0]
	v_mfma_scale_f32_16x16x128_f8f6f4 v[86:89], v[18:25], v[208:215], 0, v188, v189 op_sel_hi:[0,0,0]
	v_mfma_scale_f32_16x16x128_f8f6f4 v[78:81], v[26:33], v[216:223], 0, v188, v189 op_sel_hi:[0,0,0]
	v_mfma_scale_f32_16x16x128_f8f6f4 v[70:73], v[18:25], v[216:223], 0, v188, v189 op_sel_hi:[0,0,0]
	v_mfma_scale_f32_16x16x128_f8f6f4 v[62:65], v[26:33], v[224:231], 0, v188, v189 op_sel_hi:[0,0,0]
	v_mfma_scale_f32_16x16x128_f8f6f4 v[54:57], v[18:25], v[224:231], 0, v188, v189 op_sel_hi:[0,0,0]
	v_mfma_scale_f32_16x16x128_f8f6f4 v[46:49], v[26:33], v[232:239], 0, v188, v189 op_sel_hi:[0,0,0]
	v_mfma_scale_f32_16x16x128_f8f6f4 v[38:41], v[18:25], v[232:239], 0, v188, v189 op_sel_hi:[0,0,0]
	s_setprio 0
	s_setprio 1
	v_mfma_scale_f32_16x16x128_f8f6f4 v[90:93], v[10:17], v[208:215], 0, v188, v189 op_sel_hi:[0,0,0]
	v_mfma_scale_f32_16x16x128_f8f6f4 v[82:85], v[2:9], v[208:215], 0, v188, v189 op_sel_hi:[0,0,0]
	v_mfma_scale_f32_16x16x128_f8f6f4 v[74:77], v[10:17], v[216:223], 0, v188, v189 op_sel_hi:[0,0,0]
	v_mfma_scale_f32_16x16x128_f8f6f4 v[66:69], v[2:9], v[216:223], 0, v188, v189 op_sel_hi:[0,0,0]
	v_mfma_scale_f32_16x16x128_f8f6f4 v[58:61], v[10:17], v[224:231], 0, v188, v189 op_sel_hi:[0,0,0]
	v_mfma_scale_f32_16x16x128_f8f6f4 v[50:53], v[2:9], v[224:231], 0, v188, v189 op_sel_hi:[0,0,0]
	v_mfma_scale_f32_16x16x128_f8f6f4 v[42:45], v[10:17], v[232:239], 0, v188, v189 op_sel_hi:[0,0,0]
	v_mfma_scale_f32_16x16x128_f8f6f4 v[34:37], v[2:9], v[232:239], 0, v188, v189 op_sel_hi:[0,0,0]
	s_setprio 0
	s_barrier
	ds_read_b128 v[26:29], v194
	ds_read_b128 v[30:33], v194 offset:1024
	ds_read_b128 v[18:21], v194 offset:2048
	ds_read_b128 v[22:25], v194 offset:3072
	ds_read_b128 v[10:13], v195
	ds_read_b128 v[14:17], v195 offset:1024
	ds_read_b128 v[2:5], v195 offset:2048
	ds_read_b128 v[6:9], v195 offset:3072
	s_mov_b32 m0, s46
	ds_read_b128 v[208:211], v193 offset:32768
	ds_read_b128 v[212:215], v193 offset:33792
	ds_read_b128 v[216:219], v193 offset:34816
	ds_read_b128 v[220:223], v193 offset:35840
	ds_read_b128 v[224:227], v193 offset:36864
	ds_read_b128 v[228:231], v193 offset:37888
	ds_read_b128 v[232:235], v193 offset:38912
	ds_read_b128 v[236:239], v193 offset:39936
	v_cndmask_b32_e32 v168, v174, v201, vcc
	global_load_lds_dwordx4 v202, s[36:37]
	s_mov_b32 m0, s47
	s_nop 0
	global_load_lds_dwordx4 v168, s[36:37]
	s_waitcnt vmcnt(9)
	s_waitcnt lgkmcnt(0)
	s_barrier
	s_setprio 1
	s_waitcnt lgkmcnt(0)
	v_mfma_scale_f32_16x16x128_f8f6f4 v[154:157], v[26:33], v[208:215], v[154:157], v188, v189 op_sel_hi:[0,0,0]
	v_mfma_scale_f32_16x16x128_f8f6f4 v[150:153], v[18:25], v[208:215], v[150:153], v188, v189 op_sel_hi:[0,0,0]
	v_mfma_scale_f32_16x16x128_f8f6f4 v[142:145], v[26:33], v[216:223], v[142:145], v188, v189 op_sel_hi:[0,0,0]
	v_mfma_scale_f32_16x16x128_f8f6f4 v[134:137], v[18:25], v[216:223], v[134:137], v188, v189 op_sel_hi:[0,0,0]
	v_mfma_scale_f32_16x16x128_f8f6f4 v[126:129], v[26:33], v[224:231], v[126:129], v188, v189 op_sel_hi:[0,0,0]
	v_mfma_scale_f32_16x16x128_f8f6f4 v[118:121], v[18:25], v[224:231], v[118:121], v188, v189 op_sel_hi:[0,0,0]
	v_mfma_scale_f32_16x16x128_f8f6f4 v[110:113], v[26:33], v[232:239], v[110:113], v188, v189 op_sel_hi:[0,0,0]
	v_mfma_scale_f32_16x16x128_f8f6f4 v[102:105], v[18:25], v[232:239], v[102:105], v188, v189 op_sel_hi:[0,0,0]
	s_setprio 0
	s_setprio 1
	v_mfma_scale_f32_16x16x128_f8f6f4 v[158:161], v[10:17], v[208:215], v[158:161], v188, v189 op_sel_hi:[0,0,0]
	v_mfma_scale_f32_16x16x128_f8f6f4 v[146:149], v[2:9], v[208:215], v[146:149], v188, v189 op_sel_hi:[0,0,0]
	v_mfma_scale_f32_16x16x128_f8f6f4 v[138:141], v[10:17], v[216:223], v[138:141], v188, v189 op_sel_hi:[0,0,0]
	v_mfma_scale_f32_16x16x128_f8f6f4 v[130:133], v[2:9], v[216:223], v[130:133], v188, v189 op_sel_hi:[0,0,0]
	v_mfma_scale_f32_16x16x128_f8f6f4 v[122:125], v[10:17], v[224:231], v[122:125], v188, v189 op_sel_hi:[0,0,0]
	v_mfma_scale_f32_16x16x128_f8f6f4 v[114:117], v[2:9], v[224:231], v[114:117], v188, v189 op_sel_hi:[0,0,0]
	v_mfma_scale_f32_16x16x128_f8f6f4 v[106:109], v[10:17], v[232:239], v[106:109], v188, v189 op_sel_hi:[0,0,0]
	v_mfma_scale_f32_16x16x128_f8f6f4 v[98:101], v[2:9], v[232:239], v[98:101], v188, v189 op_sel_hi:[0,0,0]
	s_setprio 0
	s_barrier
	s_mov_b32 m0, s63
	v_lshl_add_u64 v[176:177], v[176:177], 0, s[16:17]
	ds_read_b128 v[208:211], v193 offset:49152
	ds_read_b128 v[212:215], v193 offset:50176
	ds_read_b128 v[216:219], v193 offset:51200
	ds_read_b128 v[220:223], v193 offset:52224
	ds_read_b128 v[224:227], v193 offset:53248
	ds_read_b128 v[228:231], v193 offset:54272
	ds_read_b128 v[232:235], v193 offset:55296
	ds_read_b128 v[236:239], v193 offset:56320
	global_load_lds_dwordx4 v[176:177], off
	v_lshl_add_u64 v[176:177], v[178:179], 0, s[16:17]
	s_mov_b32 m0, s64
	s_nop 0
	global_load_lds_dwordx4 v[176:177], off
	v_lshl_add_u64 v[176:177], v[180:181], 0, s[16:17]
	s_mov_b32 m0, s65
	s_nop 0
	global_load_lds_dwordx4 v[176:177], off
	v_lshl_add_u64 v[176:177], v[182:183], 0, s[16:17]
	s_mov_b32 m0, s66
	s_nop 0
	global_load_lds_dwordx4 v[176:177], off
	v_lshl_add_u64 v[176:177], v[186:187], 0, s[16:17]
	s_mov_b32 m0, s53
	s_nop 0
	global_load_lds_dwordx4 v[176:177], off
	v_lshl_add_u64 v[176:177], v[184:185], 0, s[16:17]
	s_mov_b32 m0, s54
	s_nop 0
	global_load_lds_dwordx4 v[176:177], off
	s_waitcnt vmcnt(9)
	s_waitcnt lgkmcnt(0)
	s_barrier
	s_setprio 1
	s_waitcnt lgkmcnt(0)
	v_mfma_scale_f32_16x16x128_f8f6f4 v[94:97], v[26:33], v[208:215], v[94:97], v188, v189 op_sel_hi:[0,0,0]
	v_mfma_scale_f32_16x16x128_f8f6f4 v[86:89], v[18:25], v[208:215], v[86:89], v188, v189 op_sel_hi:[0,0,0]
	v_mfma_scale_f32_16x16x128_f8f6f4 v[78:81], v[26:33], v[216:223], v[78:81], v188, v189 op_sel_hi:[0,0,0]
	v_mfma_scale_f32_16x16x128_f8f6f4 v[70:73], v[18:25], v[216:223], v[70:73], v188, v189 op_sel_hi:[0,0,0]
	v_mfma_scale_f32_16x16x128_f8f6f4 v[62:65], v[26:33], v[224:231], v[62:65], v188, v189 op_sel_hi:[0,0,0]
	v_mfma_scale_f32_16x16x128_f8f6f4 v[54:57], v[18:25], v[224:231], v[54:57], v188, v189 op_sel_hi:[0,0,0]
	v_mfma_scale_f32_16x16x128_f8f6f4 v[46:49], v[26:33], v[232:239], v[46:49], v188, v189 op_sel_hi:[0,0,0]
	v_mfma_scale_f32_16x16x128_f8f6f4 v[38:41], v[18:25], v[232:239], v[38:41], v188, v189 op_sel_hi:[0,0,0]
	s_setprio 0
	s_setprio 1
	v_mfma_scale_f32_16x16x128_f8f6f4 v[90:93], v[10:17], v[208:215], v[90:93], v188, v189 op_sel_hi:[0,0,0]
	v_mfma_scale_f32_16x16x128_f8f6f4 v[82:85], v[2:9], v[208:215], v[82:85], v188, v189 op_sel_hi:[0,0,0]
	v_mfma_scale_f32_16x16x128_f8f6f4 v[74:77], v[10:17], v[216:223], v[74:77], v188, v189 op_sel_hi:[0,0,0]
	v_mfma_scale_f32_16x16x128_f8f6f4 v[66:69], v[2:9], v[216:223], v[66:69], v188, v189 op_sel_hi:[0,0,0]
	v_mfma_scale_f32_16x16x128_f8f6f4 v[58:61], v[10:17], v[224:231], v[58:61], v188, v189 op_sel_hi:[0,0,0]
	v_mfma_scale_f32_16x16x128_f8f6f4 v[50:53], v[2:9], v[224:231], v[50:53], v188, v189 op_sel_hi:[0,0,0]
	v_mfma_scale_f32_16x16x128_f8f6f4 v[42:45], v[10:17], v[232:239], v[42:45], v188, v189 op_sel_hi:[0,0,0]
	v_mfma_scale_f32_16x16x128_f8f6f4 v[34:37], v[2:9], v[232:239], v[34:37], v188, v189 op_sel_hi:[0,0,0]
	s_setprio 0
	s_barrier
	s_add_u32 s30, s30, 0x100
	s_addc_u32 s31, s31, 0
	s_add_u32 s34, s34, 0x100
	s_addc_u32 s35, s35, 0
	s_cmp_ge_i32 s21, s52
	s_cbranch_scc1 .LBB0_1365
	s_branch .LBB0_1364
